# v35: v33 + SwiGLU epilogue: int-to-float converts and store-address computation hoisted above the scale-load wait (hides load latency), 7 fewer 64-bit mads
# speedup vs baseline: 1.0125x; 1.0043x over previous
.LBB0_1511:
	s_lshl_b32 s23, s38, 8
	s_add_i32 s23, s23, s87
	s_mul_i32 s37, s65, 0x5800
	s_mul_hi_i32 s29, s65, 0x5800
	s_add_u32 s37, s59, s37
	s_addc_u32 s29, s60, s29
	s_lshl_b32 s40, s36, 8
	s_ashr_i32 s41, s40, 31
	s_lshl_b64 s[40:41], s[40:41], 2
	s_add_u32 s37, s37, s40
	v_mbcnt_lo_u32_b32 v0, -1, 0
	v_mbcnt_hi_u32_b32 v0, -1, v0
	s_addc_u32 s29, s29, s41
	v_lshrrev_b32_e32 v82, 1, v0
	s_lshl_b32 s38, s72, 2
	v_and_or_b32 v160, v0, 15, s23
	v_and_b32_e32 v162, 24, v82
	s_add_u32 s40, s37, s38
	v_ashrrev_i32_e32 v161, 31, v160
	s_addc_u32 s41, s29, 0
	v_lshlrev_b32_e32 v90, 2, v162
	v_lshl_add_u64 v[146:147], v[160:161], 2, s[20:21]
	global_load_dwordx4 v[86:89], v90, s[40:41] offset:16
	global_load_dwordx4 v[94:97], v90, s[40:41]
	global_load_dwordx4 v[82:85], v90, s[40:41] offset:528
	s_nop 0
	global_load_dwordx4 v[90:93], v90, s[40:41] offset:512
	v_cvt_f32_i32_e32 v173, v143
	global_load_dword v170, v[146:147], off
	global_load_dword v158, v[146:147], off offset:64
	global_load_dword v156, v[146:147], off offset:128
	global_load_dword v154, v[146:147], off offset:192
	global_load_dword v152, v[146:147], off offset:512
	global_load_dword v150, v[146:147], off offset:576
	global_load_dword v148, v[146:147], off offset:640
	global_load_dword v0, v[146:147], off offset:704
	v_cvt_f32_i32_e32 v172, v142
	v_cvt_f32_i32_e32 v143, v145
	v_cvt_f32_i32_e32 v142, v144
	s_lshl_b32 s23, s36, 7
	s_or_b32 s23, s23, s72
	v_or_b32_e32 v146, s23, v162
	v_cvt_f32_i32_e32 v133, v133
	v_cvt_f32_i32_e32 v132, v132
	v_cvt_f32_i32_e32 v131, v131
	v_cvt_f32_i32_e32 v130, v130
	s_mov_b32 s23, 0xc3e00000
	s_movk_i32 s29, 0xb00
	v_cvt_f32_i32_e32 v127, v127
	v_cvt_f32_i32_e32 v126, v126
	v_ashrrev_i32_e32 v147, 31, v146
	v_mov_b64_e32 v[176:177], s[18:19]
	v_mad_i64_i32 v[176:177], s[36:37], v160, s29, v[176:177]
	v_lshl_add_u64 v[176:177], v[176:177], 0, v[146:147]
	s_mov_b32 s41, 0
	s_mov_b32 s40, 0xb000
	v_lshl_add_u64 v[178:179], v[176:177], 0, s[40:41]
	s_mov_b32 s40, 0x16000
	v_lshl_add_u64 v[180:181], v[176:177], 0, s[40:41]
	s_mov_b32 s40, 0x21000
	v_lshl_add_u64 v[182:183], v[176:177], 0, s[40:41]
	s_mov_b32 s40, 0x58000
	v_lshl_add_u64 v[184:185], v[176:177], 0, s[40:41]
	s_mov_b32 s40, 0x63000
	v_lshl_add_u64 v[186:187], v[176:177], 0, s[40:41]
	s_mov_b32 s40, 0x6e000
	v_lshl_add_u64 v[188:189], v[176:177], 0, s[40:41]
	s_mov_b32 s40, 0x79000
	v_lshl_add_u64 v[190:191], v[176:177], 0, s[40:41]
	v_cvt_f32_i32_e32 v129, v129
	v_cvt_f32_i32_e32 v128, v128
	v_cvt_f32_i32_e32 v119, v119
	v_cvt_f32_i32_e32 v118, v118
	v_cvt_f32_i32_e32 v121, v121
	v_cvt_f32_i32_e32 v120, v120
	v_cvt_f32_i32_e32 v123, v123
	v_cvt_f32_i32_e32 v122, v122
	v_cvt_f32_i32_e32 v125, v125
	v_cvt_f32_i32_e32 v124, v124
	v_cvt_f32_i32_e32 v115, v115
	v_cvt_f32_i32_e32 v114, v114
	v_cvt_f32_i32_e32 v117, v117
	v_cvt_f32_i32_e32 v116, v116
	v_cvt_f32_i32_e32 v111, v111
	v_cvt_f32_i32_e32 v110, v110
	v_cvt_f32_i32_e32 v113, v113
	v_cvt_f32_i32_e32 v112, v112
	v_cvt_f32_i32_e32 v103, v103
	v_cvt_f32_i32_e32 v102, v102
	v_cvt_f32_i32_e32 v105, v105
	v_cvt_f32_i32_e32 v104, v104
	v_cvt_f32_i32_e32 v107, v107
	v_cvt_f32_i32_e32 v106, v106
	v_cvt_f32_i32_e32 v109, v109
	v_cvt_f32_i32_e32 v108, v108
	v_cvt_f32_i32_e32 v99, v99
	v_cvt_f32_i32_e32 v98, v98
	v_cvt_f32_i32_e32 v101, v101
	v_cvt_f32_i32_e32 v100, v100
	v_cvt_f32_i32_e32 v79, v79
	v_cvt_f32_i32_e32 v78, v78
	v_cvt_f32_i32_e32 v81, v81
	v_cvt_f32_i32_e32 v80, v80
	v_cvt_f32_i32_e32 v71, v71
	v_cvt_f32_i32_e32 v70, v70
	v_cvt_f32_i32_e32 v73, v73
	v_cvt_f32_i32_e32 v72, v72
	v_cvt_f32_i32_e32 v75, v75
	v_cvt_f32_i32_e32 v74, v74
	v_cvt_f32_i32_e32 v77, v77
	v_cvt_f32_i32_e32 v76, v76
	v_cvt_f32_i32_e32 v67, v67
	v_cvt_f32_i32_e32 v66, v66
	v_cvt_f32_i32_e32 v69, v69
	v_cvt_f32_i32_e32 v68, v68
	v_cvt_f32_i32_e32 v63, v63
	v_cvt_f32_i32_e32 v62, v62
	v_cvt_f32_i32_e32 v65, v65
	v_cvt_f32_i32_e32 v64, v64
	v_cvt_f32_i32_e32 v55, v55
	v_cvt_f32_i32_e32 v54, v54
	v_cvt_f32_i32_e32 v57, v57
	v_cvt_f32_i32_e32 v56, v56
	v_cvt_f32_i32_e32 v59, v59
	v_cvt_f32_i32_e32 v58, v58
	v_cvt_f32_i32_e32 v61, v61
	v_cvt_f32_i32_e32 v60, v60
	v_cvt_f32_i32_e32 v51, v51
	v_cvt_f32_i32_e32 v50, v50
	v_cvt_f32_i32_e32 v53, v53
	v_cvt_f32_i32_e32 v52, v52
	v_cvt_f32_i32_e32 v47, v47
	v_cvt_f32_i32_e32 v46, v46
	v_cvt_f32_i32_e32 v49, v49
	v_cvt_f32_i32_e32 v48, v48
	v_cvt_f32_i32_e32 v39, v39
	v_cvt_f32_i32_e32 v38, v38
	v_cvt_f32_i32_e32 v41, v41
	v_cvt_f32_i32_e32 v40, v40
	v_cvt_f32_i32_e32 v43, v43
	v_cvt_f32_i32_e32 v42, v42
	v_cvt_f32_i32_e32 v45, v45
	v_cvt_f32_i32_e32 v44, v44
	v_cvt_f32_i32_e32 v35, v35
	v_cvt_f32_i32_e32 v34, v34
	v_cvt_f32_i32_e32 v37, v37
	v_cvt_f32_i32_e32 v36, v36
	v_cvt_f32_i32_e32 v31, v31
	v_cvt_f32_i32_e32 v30, v30
	v_cvt_f32_i32_e32 v33, v33
	v_cvt_f32_i32_e32 v32, v32
	v_cvt_f32_i32_e32 v23, v23
	v_cvt_f32_i32_e32 v22, v22
	v_cvt_f32_i32_e32 v25, v25
	v_cvt_f32_i32_e32 v24, v24
	v_cvt_f32_i32_e32 v27, v27
	v_cvt_f32_i32_e32 v26, v26
	v_cvt_f32_i32_e32 v29, v29
	v_cvt_f32_i32_e32 v28, v28
	v_cvt_f32_i32_e32 v19, v19
	v_cvt_f32_i32_e32 v18, v18
	v_cvt_f32_i32_e32 v21, v21
	v_cvt_f32_i32_e32 v20, v20
	v_cvt_f32_i32_e32 v17, v17
	v_cvt_f32_i32_e32 v16, v16
	v_cvt_f32_i32_e32 v15, v15
	v_cvt_f32_i32_e32 v14, v14
	v_cvt_f32_i32_e32 v9, v9
	v_cvt_f32_i32_e32 v8, v8
	v_cvt_f32_i32_e32 v7, v7
	v_cvt_f32_i32_e32 v6, v6
	v_cvt_f32_i32_e32 v13, v13
	v_cvt_f32_i32_e32 v12, v12
	v_cvt_f32_i32_e32 v3, v3
	v_cvt_f32_i32_e32 v2, v2
	v_cvt_f32_i32_e32 v11, v11
	v_cvt_f32_i32_e32 v10, v10
	v_cvt_f32_i32_e32 v5, v5
	v_cvt_f32_i32_e32 v4, v4
	s_waitcnt vmcnt(0)
	v_mul_f32_e32 v94, 0x3fb8aa3b, v94
	v_mul_f32_e32 v95, 0x3fb8aa3b, v95
	v_mul_f32_e32 v96, 0x3fb8aa3b, v96
	v_mul_f32_e32 v97, 0x3fb8aa3b, v97
	v_mul_f32_e32 v86, 0x3fb8aa3b, v86
	v_mul_f32_e32 v87, 0x3fb8aa3b, v87
	v_mul_f32_e32 v88, 0x3fb8aa3b, v88
	v_mul_f32_e32 v89, 0x3fb8aa3b, v89
	v_mul_f32_e32 v90, 0x3f317218, v90
	v_mul_f32_e32 v91, 0x3f317218, v91
	v_mul_f32_e32 v92, 0x3f317218, v92
	v_mul_f32_e32 v93, 0x3f317218, v93
	v_mul_f32_e32 v82, 0x3f317218, v82
	v_mul_f32_e32 v83, 0x3f317218, v83
	v_mul_f32_e32 v84, 0x3f317218, v84
	v_mul_f32_e32 v85, 0x3f317218, v85
	v_pk_mul_f32 v[144:145], v[96:97], v[170:171] op_sel_hi:[1,0]
	v_pk_mul_f32 v[174:175], v[94:95], v[170:171] op_sel_hi:[1,0]
	v_pk_mul_f32 v[142:143], v[144:145], v[142:143]
	v_pk_mul_f32 v[144:145], v[174:175], v[172:173]
	v_cvt_f32_i32_e32 v173, v139
	v_cvt_f32_i32_e32 v172, v138
	v_cvt_f32_i32_e32 v139, v141
	v_cvt_f32_i32_e32 v138, v140
	v_mul_f32_e32 v162, 4.0, v170
	v_pk_mul_f32 v[140:141], v[92:93], v[162:163] op_sel_hi:[1,0]
	v_pk_mul_f32 v[174:175], v[90:91], v[162:163] op_sel_hi:[1,0]
	v_pk_mul_f32 v[138:139], v[140:141], v[138:139]
	v_pk_mul_f32 v[140:141], v[174:175], v[172:173]
	v_cvt_f32_i32_e32 v173, v135
	v_cvt_f32_i32_e32 v172, v134
	v_cvt_f32_i32_e32 v135, v137
	v_cvt_f32_i32_e32 v134, v136
	v_pk_mul_f32 v[136:137], v[88:89], v[170:171] op_sel_hi:[1,0]
	v_pk_mul_f32 v[170:171], v[86:87], v[170:171] op_sel_hi:[1,0]
	v_pk_mul_f32 v[134:135], v[136:137], v[134:135]
	v_pk_mul_f32 v[136:137], v[170:171], v[172:173]
	v_pk_mul_f32 v[170:171], v[84:85], v[162:163] op_sel_hi:[1,0]
	v_pk_mul_f32 v[172:173], v[82:83], v[162:163] op_sel_hi:[1,0]
	v_pk_mul_f32 v[132:133], v[170:171], v[132:133]
	v_pk_mul_f32 v[130:131], v[172:173], v[130:131]
	v_exp_f32_e64 v162, -v144
	v_exp_f32_e64 v170, -v142
	v_exp_f32_e64 v169, -v145
	v_exp_f32_e64 v171, -v143
	v_exp_f32_e64 v172, -v136
	v_exp_f32_e64 v174, -v134
	v_exp_f32_e64 v173, -v137
	v_exp_f32_e64 v175, -v135
	v_add_f32_e32 v162, 1.0, v162
	v_add_f32_e32 v170, 1.0, v170
	v_rcp_f32_e32 v162, v162
	v_add_f32_e32 v169, 1.0, v169
	v_rcp_f32_e32 v170, v170
	v_add_f32_e32 v171, 1.0, v171
	v_add_f32_e32 v172, 1.0, v172
	v_add_f32_e32 v174, 1.0, v174
	v_rcp_f32_e32 v169, v169
	v_rcp_f32_e32 v171, v171
	v_rcp_f32_e32 v172, v172
	v_add_f32_e32 v173, 1.0, v173
	v_rcp_f32_e32 v174, v174
	v_add_f32_e32 v175, 1.0, v175
	v_rcp_f32_e32 v173, v173
	v_rcp_f32_e32 v175, v175
	v_mul_f32_e32 v144, v144, v162
	v_mul_f32_e32 v142, v142, v170
	v_mul_f32_e32 v140, v140, v144
	v_mul_f32_e32 v144, v145, v169
	v_mul_f32_e32 v138, v138, v142
	v_mul_f32_e32 v142, v143, v171
	v_mul_f32_e32 v136, v136, v172
	v_mul_f32_e32 v134, v134, v174
	v_mul_f32_e32 v141, v141, v144
	v_mul_f32_e32 v139, v139, v142
	v_mul_f32_e32 v130, v130, v136
	v_mul_f32_e32 v136, v137, v173
	v_mul_f32_e32 v134, v132, v134
	v_mul_f32_e32 v132, v135, v175
	v_mov_b32_e32 v142, 0x43e00000
	v_mul_f32_e32 v131, v131, v136
	v_mul_f32_e32 v133, v133, v132
	v_med3_f32 v135, v140, s23, v142
	v_med3_f32 v136, v141, s23, v142
	v_cvt_pk_fp8_f32 v132, v135, v136
	v_med3_f32 v130, v130, s23, v142
	v_med3_f32 v131, v131, s23, v142
	v_med3_f32 v135, v133, s23, v142
	v_cvt_pk_fp8_f32 v133, v130, v131
	v_med3_f32 v137, v138, s23, v142
	v_med3_f32 v138, v139, s23, v142
	v_med3_f32 v134, v134, s23, v142
	v_cvt_pk_fp8_f32 v132, v137, v138 op_sel:[0,0,1]
	v_cvt_pk_fp8_f32 v133, v134, v135 op_sel:[0,0,1]
	global_store_dwordx2 v[176:177], v[132:133], off
	v_mul_f32_e32 v132, 4.0, v158
	v_pk_mul_f32 v[136:137], v[94:95], v[158:159] op_sel_hi:[1,0]
	v_pk_mul_f32 v[134:135], v[96:97], v[158:159] op_sel_hi:[1,0]
	v_pk_mul_f32 v[126:127], v[136:137], v[126:127]
	v_pk_mul_f32 v[136:137], v[90:91], v[132:133] op_sel_hi:[1,0]
	v_pk_mul_f32 v[128:129], v[134:135], v[128:129]
	v_pk_mul_f32 v[134:135], v[92:93], v[132:133] op_sel_hi:[1,0]
	v_pk_mul_f32 v[118:119], v[136:137], v[118:119]
	v_pk_mul_f32 v[136:137], v[86:87], v[158:159] op_sel_hi:[1,0]
	v_pk_mul_f32 v[120:121], v[134:135], v[120:121]
	v_pk_mul_f32 v[134:135], v[88:89], v[158:159] op_sel_hi:[1,0]
	v_pk_mul_f32 v[122:123], v[136:137], v[122:123]
	v_pk_mul_f32 v[124:125], v[134:135], v[124:125]
	v_pk_mul_f32 v[134:135], v[84:85], v[132:133] op_sel_hi:[1,0]
	v_pk_mul_f32 v[132:133], v[82:83], v[132:133] op_sel_hi:[1,0]
	v_pk_mul_f32 v[114:115], v[132:133], v[114:115]
	v_exp_f32_e64 v136, -v122
	v_exp_f32_e64 v132, -v126
	v_exp_f32_e64 v137, -v123
	v_exp_f32_e64 v133, -v127
	v_exp_f32_e64 v138, -v124
	v_exp_f32_e64 v139, -v125
	v_add_f32_e32 v136, 1.0, v136
	v_pk_mul_f32 v[116:117], v[134:135], v[116:117]
	v_add_f32_e32 v132, 1.0, v132
	v_rcp_f32_e32 v136, v136
	v_add_f32_e32 v137, 1.0, v137
	v_exp_f32_e64 v134, -v128
	v_rcp_f32_e32 v132, v132
	v_add_f32_e32 v133, 1.0, v133
	v_rcp_f32_e32 v137, v137
	v_add_f32_e32 v138, 1.0, v138
	v_exp_f32_e64 v135, -v129
	v_rcp_f32_e32 v133, v133
	v_rcp_f32_e32 v138, v138
	v_add_f32_e32 v139, 1.0, v139
	v_rcp_f32_e32 v139, v139
	v_mul_f32_e32 v122, v122, v136
	v_add_f32_e32 v134, 1.0, v134
	v_mul_f32_e32 v126, v126, v132
	v_mul_f32_e32 v122, v114, v122
	v_mul_f32_e32 v114, v123, v137
	v_rcp_f32_e32 v134, v134
	v_add_f32_e32 v135, 1.0, v135
	v_mul_f32_e32 v118, v118, v126
	v_mul_f32_e32 v126, v127, v133
	v_mul_f32_e32 v115, v115, v114
	v_mul_f32_e32 v114, v124, v138
	v_rcp_f32_e32 v135, v135
	v_mul_f32_e32 v119, v119, v126
	v_mul_f32_e32 v116, v116, v114
	v_mul_f32_e32 v114, v125, v139
	v_mul_f32_e32 v117, v117, v114
	v_med3_f32 v118, v118, s23, v142
	v_med3_f32 v119, v119, s23, v142
	v_cvt_pk_fp8_f32 v114, v118, v119
	v_med3_f32 v118, v122, s23, v142
	v_med3_f32 v119, v115, s23, v142
	v_mul_f32_e32 v126, v128, v134
	v_cvt_pk_fp8_f32 v115, v118, v119
	v_mul_f32_e32 v120, v120, v126
	v_mul_f32_e32 v126, v129, v135
	v_mul_f32_e32 v121, v121, v126
	v_med3_f32 v120, v120, s23, v142
	v_med3_f32 v121, v121, s23, v142
	v_med3_f32 v116, v116, s23, v142
	v_med3_f32 v117, v117, s23, v142
	v_cvt_pk_fp8_f32 v114, v120, v121 op_sel:[0,0,1]
	v_cvt_pk_fp8_f32 v115, v116, v117 op_sel:[0,0,1]
	global_store_dwordx2 v[178:179], v[114:115], off
	v_mul_f32_e32 v114, 4.0, v156
	v_pk_mul_f32 v[118:119], v[94:95], v[156:157] op_sel_hi:[1,0]
	v_pk_mul_f32 v[116:117], v[96:97], v[156:157] op_sel_hi:[1,0]
	v_pk_mul_f32 v[110:111], v[118:119], v[110:111]
	v_pk_mul_f32 v[118:119], v[90:91], v[114:115] op_sel_hi:[1,0]
	v_pk_mul_f32 v[112:113], v[116:117], v[112:113]
	v_pk_mul_f32 v[116:117], v[92:93], v[114:115] op_sel_hi:[1,0]
	v_pk_mul_f32 v[102:103], v[118:119], v[102:103]
	v_pk_mul_f32 v[118:119], v[86:87], v[156:157] op_sel_hi:[1,0]
	v_pk_mul_f32 v[104:105], v[116:117], v[104:105]
	v_pk_mul_f32 v[116:117], v[88:89], v[156:157] op_sel_hi:[1,0]
	v_pk_mul_f32 v[106:107], v[118:119], v[106:107]
	v_pk_mul_f32 v[108:109], v[116:117], v[108:109]
	v_pk_mul_f32 v[116:117], v[84:85], v[114:115] op_sel_hi:[1,0]
	v_pk_mul_f32 v[114:115], v[82:83], v[114:115] op_sel_hi:[1,0]
	v_pk_mul_f32 v[98:99], v[114:115], v[98:99]
	v_exp_f32_e64 v118, -v106
	v_exp_f32_e64 v114, -v110
	v_exp_f32_e64 v119, -v107
	v_exp_f32_e64 v115, -v111
	v_exp_f32_e64 v120, -v108
	v_exp_f32_e64 v121, -v109
	v_add_f32_e32 v118, 1.0, v118
	v_pk_mul_f32 v[100:101], v[116:117], v[100:101]
	v_add_f32_e32 v114, 1.0, v114
	v_rcp_f32_e32 v118, v118
	v_add_f32_e32 v119, 1.0, v119
	v_exp_f32_e64 v116, -v112
	v_rcp_f32_e32 v114, v114
	v_add_f32_e32 v115, 1.0, v115
	v_rcp_f32_e32 v119, v119
	v_add_f32_e32 v120, 1.0, v120
	v_exp_f32_e64 v117, -v113
	v_rcp_f32_e32 v115, v115
	v_rcp_f32_e32 v120, v120
	v_add_f32_e32 v121, 1.0, v121
	v_rcp_f32_e32 v121, v121
	v_mul_f32_e32 v106, v106, v118
	v_add_f32_e32 v116, 1.0, v116
	v_mul_f32_e32 v110, v110, v114
	v_mul_f32_e32 v106, v98, v106
	v_mul_f32_e32 v98, v107, v119
	v_rcp_f32_e32 v116, v116
	v_add_f32_e32 v117, 1.0, v117
	v_mul_f32_e32 v102, v102, v110
	v_mul_f32_e32 v110, v111, v115
	v_mul_f32_e32 v99, v99, v98
	v_mul_f32_e32 v98, v108, v120
	v_rcp_f32_e32 v117, v117
	v_mul_f32_e32 v103, v103, v110
	v_mul_f32_e32 v100, v100, v98
	v_mul_f32_e32 v98, v109, v121
	v_mul_f32_e32 v101, v101, v98
	v_med3_f32 v102, v102, s23, v142
	v_med3_f32 v103, v103, s23, v142
	v_cvt_pk_fp8_f32 v98, v102, v103
	v_med3_f32 v102, v106, s23, v142
	v_med3_f32 v103, v99, s23, v142
	v_mul_f32_e32 v110, v112, v116
	v_cvt_pk_fp8_f32 v99, v102, v103
	v_mul_f32_e32 v104, v104, v110
	v_mul_f32_e32 v110, v113, v117
	v_mul_f32_e32 v105, v105, v110
	v_med3_f32 v104, v104, s23, v142
	v_med3_f32 v105, v105, s23, v142
	v_med3_f32 v100, v100, s23, v142
	v_med3_f32 v101, v101, s23, v142
	v_cvt_pk_fp8_f32 v98, v104, v105 op_sel:[0,0,1]
	v_cvt_pk_fp8_f32 v99, v100, v101 op_sel:[0,0,1]
	global_store_dwordx2 v[180:181], v[98:99], off
	v_mul_f32_e32 v98, 4.0, v154
	v_pk_mul_f32 v[102:103], v[94:95], v[154:155] op_sel_hi:[1,0]
	v_pk_mul_f32 v[100:101], v[96:97], v[154:155] op_sel_hi:[1,0]
	v_pk_mul_f32 v[78:79], v[102:103], v[78:79]
	v_pk_mul_f32 v[102:103], v[90:91], v[98:99] op_sel_hi:[1,0]
	v_pk_mul_f32 v[80:81], v[100:101], v[80:81]
	v_pk_mul_f32 v[100:101], v[92:93], v[98:99] op_sel_hi:[1,0]
	v_pk_mul_f32 v[70:71], v[102:103], v[70:71]
	v_pk_mul_f32 v[102:103], v[86:87], v[154:155] op_sel_hi:[1,0]
	v_pk_mul_f32 v[72:73], v[100:101], v[72:73]
	v_pk_mul_f32 v[100:101], v[88:89], v[154:155] op_sel_hi:[1,0]
	v_pk_mul_f32 v[74:75], v[102:103], v[74:75]
	v_pk_mul_f32 v[76:77], v[100:101], v[76:77]
	v_pk_mul_f32 v[100:101], v[84:85], v[98:99] op_sel_hi:[1,0]
	v_pk_mul_f32 v[98:99], v[82:83], v[98:99] op_sel_hi:[1,0]
	v_pk_mul_f32 v[66:67], v[98:99], v[66:67]
	v_exp_f32_e64 v102, -v74
	v_exp_f32_e64 v98, -v78
	v_exp_f32_e64 v103, -v75
	v_exp_f32_e64 v99, -v79
	v_exp_f32_e64 v104, -v76
	v_exp_f32_e64 v105, -v77
	v_add_f32_e32 v102, 1.0, v102
	v_pk_mul_f32 v[68:69], v[100:101], v[68:69]
	v_add_f32_e32 v98, 1.0, v98
	v_rcp_f32_e32 v102, v102
	v_add_f32_e32 v103, 1.0, v103
	v_exp_f32_e64 v100, -v80
	v_rcp_f32_e32 v98, v98
	v_add_f32_e32 v99, 1.0, v99
	v_rcp_f32_e32 v103, v103
	v_add_f32_e32 v104, 1.0, v104
	v_exp_f32_e64 v101, -v81
	v_rcp_f32_e32 v99, v99
	v_rcp_f32_e32 v104, v104
	v_add_f32_e32 v105, 1.0, v105
	v_rcp_f32_e32 v105, v105
	v_mul_f32_e32 v74, v74, v102
	v_add_f32_e32 v100, 1.0, v100
	v_mul_f32_e32 v78, v78, v98
	v_mul_f32_e32 v74, v66, v74
	v_mul_f32_e32 v66, v75, v103
	v_rcp_f32_e32 v100, v100
	v_add_f32_e32 v101, 1.0, v101
	v_mul_f32_e32 v70, v70, v78
	v_mul_f32_e32 v78, v79, v99
	v_mul_f32_e32 v67, v67, v66
	v_mul_f32_e32 v66, v76, v104
	v_rcp_f32_e32 v101, v101
	v_mul_f32_e32 v71, v71, v78
	v_mul_f32_e32 v68, v68, v66
	v_mul_f32_e32 v66, v77, v105
	v_mul_f32_e32 v69, v69, v66
	v_med3_f32 v70, v70, s23, v142
	v_med3_f32 v71, v71, s23, v142
	v_cvt_pk_fp8_f32 v66, v70, v71
	v_med3_f32 v70, v74, s23, v142
	v_med3_f32 v71, v67, s23, v142
	v_mul_f32_e32 v78, v80, v100
	v_cvt_pk_fp8_f32 v67, v70, v71
	v_mul_f32_e32 v72, v72, v78
	v_mul_f32_e32 v78, v81, v101
	v_mul_f32_e32 v73, v73, v78
	v_med3_f32 v72, v72, s23, v142
	v_med3_f32 v73, v73, s23, v142
	v_med3_f32 v68, v68, s23, v142
	v_med3_f32 v69, v69, s23, v142
	v_cvt_pk_fp8_f32 v66, v72, v73 op_sel:[0,0,1]
	v_cvt_pk_fp8_f32 v67, v68, v69 op_sel:[0,0,1]
	global_store_dwordx2 v[182:183], v[66:67], off
	v_mul_f32_e32 v66, 4.0, v152
	v_pk_mul_f32 v[70:71], v[94:95], v[152:153] op_sel_hi:[1,0]
	v_pk_mul_f32 v[68:69], v[96:97], v[152:153] op_sel_hi:[1,0]
	v_pk_mul_f32 v[62:63], v[70:71], v[62:63]
	v_pk_mul_f32 v[70:71], v[90:91], v[66:67] op_sel_hi:[1,0]
	v_pk_mul_f32 v[64:65], v[68:69], v[64:65]
	v_pk_mul_f32 v[68:69], v[92:93], v[66:67] op_sel_hi:[1,0]
	v_pk_mul_f32 v[54:55], v[70:71], v[54:55]
	v_pk_mul_f32 v[70:71], v[86:87], v[152:153] op_sel_hi:[1,0]
	v_pk_mul_f32 v[56:57], v[68:69], v[56:57]
	v_pk_mul_f32 v[68:69], v[88:89], v[152:153] op_sel_hi:[1,0]
	v_pk_mul_f32 v[58:59], v[70:71], v[58:59]
	v_pk_mul_f32 v[60:61], v[68:69], v[60:61]
	v_pk_mul_f32 v[68:69], v[84:85], v[66:67] op_sel_hi:[1,0]
	v_pk_mul_f32 v[66:67], v[82:83], v[66:67] op_sel_hi:[1,0]
	v_pk_mul_f32 v[50:51], v[66:67], v[50:51]
	v_exp_f32_e64 v70, -v58
	v_exp_f32_e64 v66, -v62
	v_exp_f32_e64 v71, -v59
	v_exp_f32_e64 v67, -v63
	v_exp_f32_e64 v72, -v60
	v_exp_f32_e64 v73, -v61
	v_add_f32_e32 v70, 1.0, v70
	v_pk_mul_f32 v[52:53], v[68:69], v[52:53]
	v_add_f32_e32 v66, 1.0, v66
	v_rcp_f32_e32 v70, v70
	v_add_f32_e32 v71, 1.0, v71
	v_exp_f32_e64 v68, -v64
	v_rcp_f32_e32 v66, v66
	v_add_f32_e32 v67, 1.0, v67
	v_rcp_f32_e32 v71, v71
	v_add_f32_e32 v72, 1.0, v72
	v_exp_f32_e64 v69, -v65
	v_rcp_f32_e32 v67, v67
	v_rcp_f32_e32 v72, v72
	v_add_f32_e32 v73, 1.0, v73
	v_rcp_f32_e32 v73, v73
	v_mul_f32_e32 v58, v58, v70
	v_add_f32_e32 v68, 1.0, v68
	v_mul_f32_e32 v62, v62, v66
	v_mul_f32_e32 v58, v50, v58
	v_mul_f32_e32 v50, v59, v71
	v_rcp_f32_e32 v68, v68
	v_add_f32_e32 v69, 1.0, v69
	v_mul_f32_e32 v54, v54, v62
	v_mul_f32_e32 v62, v63, v67
	v_mul_f32_e32 v51, v51, v50
	v_mul_f32_e32 v50, v60, v72
	v_rcp_f32_e32 v69, v69
	v_mul_f32_e32 v55, v55, v62
	v_mul_f32_e32 v52, v52, v50
	v_mul_f32_e32 v50, v61, v73
	v_mul_f32_e32 v53, v53, v50
	v_med3_f32 v54, v54, s23, v142
	v_med3_f32 v55, v55, s23, v142
	v_cvt_pk_fp8_f32 v50, v54, v55
	v_med3_f32 v54, v58, s23, v142
	v_med3_f32 v55, v51, s23, v142
	v_mul_f32_e32 v62, v64, v68
	v_cvt_pk_fp8_f32 v51, v54, v55
	v_mul_f32_e32 v56, v56, v62
	v_mul_f32_e32 v62, v65, v69
	v_mul_f32_e32 v57, v57, v62
	v_med3_f32 v56, v56, s23, v142
	v_med3_f32 v57, v57, s23, v142
	v_med3_f32 v52, v52, s23, v142
	v_med3_f32 v53, v53, s23, v142
	v_cvt_pk_fp8_f32 v50, v56, v57 op_sel:[0,0,1]
	v_cvt_pk_fp8_f32 v51, v52, v53 op_sel:[0,0,1]
	global_store_dwordx2 v[184:185], v[50:51], off
	v_mul_f32_e32 v50, 4.0, v150
	v_pk_mul_f32 v[54:55], v[94:95], v[150:151] op_sel_hi:[1,0]
	v_pk_mul_f32 v[52:53], v[96:97], v[150:151] op_sel_hi:[1,0]
	v_pk_mul_f32 v[46:47], v[54:55], v[46:47]
	v_pk_mul_f32 v[54:55], v[90:91], v[50:51] op_sel_hi:[1,0]
	v_pk_mul_f32 v[48:49], v[52:53], v[48:49]
	v_pk_mul_f32 v[52:53], v[92:93], v[50:51] op_sel_hi:[1,0]
	v_pk_mul_f32 v[38:39], v[54:55], v[38:39]
	v_pk_mul_f32 v[54:55], v[86:87], v[150:151] op_sel_hi:[1,0]
	v_pk_mul_f32 v[40:41], v[52:53], v[40:41]
	v_pk_mul_f32 v[52:53], v[88:89], v[150:151] op_sel_hi:[1,0]
	v_pk_mul_f32 v[42:43], v[54:55], v[42:43]
	v_pk_mul_f32 v[44:45], v[52:53], v[44:45]
	v_pk_mul_f32 v[52:53], v[84:85], v[50:51] op_sel_hi:[1,0]
	v_pk_mul_f32 v[50:51], v[82:83], v[50:51] op_sel_hi:[1,0]
	v_pk_mul_f32 v[34:35], v[50:51], v[34:35]
	v_exp_f32_e64 v54, -v42
	v_exp_f32_e64 v50, -v46
	v_exp_f32_e64 v55, -v43
	v_exp_f32_e64 v51, -v47
	v_exp_f32_e64 v56, -v44
	v_exp_f32_e64 v57, -v45
	v_add_f32_e32 v54, 1.0, v54
	v_pk_mul_f32 v[36:37], v[52:53], v[36:37]
	v_add_f32_e32 v50, 1.0, v50
	v_rcp_f32_e32 v54, v54
	v_add_f32_e32 v55, 1.0, v55
	v_exp_f32_e64 v52, -v48
	v_rcp_f32_e32 v50, v50
	v_add_f32_e32 v51, 1.0, v51
	v_rcp_f32_e32 v55, v55
	v_add_f32_e32 v56, 1.0, v56
	v_exp_f32_e64 v53, -v49
	v_rcp_f32_e32 v51, v51
	v_rcp_f32_e32 v56, v56
	v_add_f32_e32 v57, 1.0, v57
	v_rcp_f32_e32 v57, v57
	v_mul_f32_e32 v42, v42, v54
	v_add_f32_e32 v52, 1.0, v52
	v_mul_f32_e32 v46, v46, v50
	v_mul_f32_e32 v42, v34, v42
	v_mul_f32_e32 v34, v43, v55
	v_rcp_f32_e32 v52, v52
	v_add_f32_e32 v53, 1.0, v53
	v_mul_f32_e32 v38, v38, v46
	v_mul_f32_e32 v46, v47, v51
	v_mul_f32_e32 v35, v35, v34
	v_mul_f32_e32 v34, v44, v56
	v_rcp_f32_e32 v53, v53
	v_mul_f32_e32 v39, v39, v46
	v_mul_f32_e32 v36, v36, v34
	v_mul_f32_e32 v34, v45, v57
	v_mul_f32_e32 v37, v37, v34
	v_med3_f32 v38, v38, s23, v142
	v_med3_f32 v39, v39, s23, v142
	v_cvt_pk_fp8_f32 v34, v38, v39
	v_med3_f32 v38, v42, s23, v142
	v_med3_f32 v39, v35, s23, v142
	v_mul_f32_e32 v46, v48, v52
	v_cvt_pk_fp8_f32 v35, v38, v39
	v_mul_f32_e32 v40, v40, v46
	v_mul_f32_e32 v46, v49, v53
	v_mul_f32_e32 v41, v41, v46
	v_med3_f32 v40, v40, s23, v142
	v_med3_f32 v41, v41, s23, v142
	v_med3_f32 v36, v36, s23, v142
	v_med3_f32 v37, v37, s23, v142
	v_cvt_pk_fp8_f32 v34, v40, v41 op_sel:[0,0,1]
	v_cvt_pk_fp8_f32 v35, v36, v37 op_sel:[0,0,1]
	global_store_dwordx2 v[186:187], v[34:35], off
	v_mul_f32_e32 v34, 4.0, v148
	v_pk_mul_f32 v[38:39], v[94:95], v[148:149] op_sel_hi:[1,0]
	v_pk_mul_f32 v[36:37], v[96:97], v[148:149] op_sel_hi:[1,0]
	v_pk_mul_f32 v[30:31], v[38:39], v[30:31]
	v_pk_mul_f32 v[38:39], v[90:91], v[34:35] op_sel_hi:[1,0]
	v_pk_mul_f32 v[32:33], v[36:37], v[32:33]
	v_pk_mul_f32 v[36:37], v[92:93], v[34:35] op_sel_hi:[1,0]
	v_pk_mul_f32 v[22:23], v[38:39], v[22:23]
	v_pk_mul_f32 v[38:39], v[86:87], v[148:149] op_sel_hi:[1,0]
	v_pk_mul_f32 v[24:25], v[36:37], v[24:25]
	v_pk_mul_f32 v[36:37], v[88:89], v[148:149] op_sel_hi:[1,0]
	v_pk_mul_f32 v[26:27], v[38:39], v[26:27]
	v_pk_mul_f32 v[28:29], v[36:37], v[28:29]
	v_pk_mul_f32 v[36:37], v[84:85], v[34:35] op_sel_hi:[1,0]
	v_pk_mul_f32 v[34:35], v[82:83], v[34:35] op_sel_hi:[1,0]
	v_pk_mul_f32 v[18:19], v[34:35], v[18:19]
	v_exp_f32_e64 v38, -v26
	v_exp_f32_e64 v34, -v30
	v_exp_f32_e64 v39, -v27
	v_exp_f32_e64 v35, -v31
	v_exp_f32_e64 v40, -v28
	v_exp_f32_e64 v41, -v29
	v_add_f32_e32 v38, 1.0, v38
	v_pk_mul_f32 v[20:21], v[36:37], v[20:21]
	v_add_f32_e32 v34, 1.0, v34
	v_rcp_f32_e32 v38, v38
	v_add_f32_e32 v39, 1.0, v39
	v_exp_f32_e64 v36, -v32
	v_rcp_f32_e32 v34, v34
	v_add_f32_e32 v35, 1.0, v35
	v_rcp_f32_e32 v39, v39
	v_add_f32_e32 v40, 1.0, v40
	v_exp_f32_e64 v37, -v33
	v_rcp_f32_e32 v35, v35
	v_rcp_f32_e32 v40, v40
	v_add_f32_e32 v41, 1.0, v41
	v_rcp_f32_e32 v41, v41
	v_mul_f32_e32 v26, v26, v38
	v_add_f32_e32 v36, 1.0, v36
	v_mul_f32_e32 v30, v30, v34
	v_mul_f32_e32 v26, v18, v26
	v_mul_f32_e32 v18, v27, v39
	v_rcp_f32_e32 v36, v36
	v_add_f32_e32 v37, 1.0, v37
	v_mul_f32_e32 v22, v22, v30
	v_mul_f32_e32 v30, v31, v35
	v_mul_f32_e32 v19, v19, v18
	v_mul_f32_e32 v18, v28, v40
	v_rcp_f32_e32 v37, v37
	v_mul_f32_e32 v23, v23, v30
	v_mul_f32_e32 v20, v20, v18
	v_mul_f32_e32 v18, v29, v41
	v_mul_f32_e32 v21, v21, v18
	v_med3_f32 v22, v22, s23, v142
	v_med3_f32 v23, v23, s23, v142
	v_cvt_pk_fp8_f32 v18, v22, v23
	v_med3_f32 v22, v26, s23, v142
	v_med3_f32 v23, v19, s23, v142
	v_mul_f32_e32 v30, v32, v36
	v_cvt_pk_fp8_f32 v19, v22, v23
	v_mul_f32_e32 v24, v24, v30
	v_mul_f32_e32 v30, v33, v37
	v_mul_f32_e32 v25, v25, v30
	v_med3_f32 v24, v24, s23, v142
	v_med3_f32 v25, v25, s23, v142
	v_med3_f32 v20, v20, s23, v142
	v_med3_f32 v21, v21, s23, v142
	v_cvt_pk_fp8_f32 v18, v24, v25 op_sel:[0,0,1]
	v_cvt_pk_fp8_f32 v19, v20, v21 op_sel:[0,0,1]
	global_store_dwordx2 v[188:189], v[18:19], off
	v_mul_f32_e32 v18, 4.0, v0
	v_pk_mul_f32 v[20:21], v[96:97], v[0:1] op_sel_hi:[1,0]
	v_pk_mul_f32 v[22:23], v[94:95], v[0:1] op_sel_hi:[1,0]
	v_pk_mul_f32 v[16:17], v[20:21], v[16:17]
	v_pk_mul_f32 v[20:21], v[92:93], v[18:19] op_sel_hi:[1,0]
	v_pk_mul_f32 v[14:15], v[22:23], v[14:15]
	v_pk_mul_f32 v[22:23], v[90:91], v[18:19] op_sel_hi:[1,0]
	v_pk_mul_f32 v[8:9], v[20:21], v[8:9]
	v_pk_mul_f32 v[20:21], v[88:89], v[0:1] op_sel_hi:[1,0]
	v_pk_mul_f32 v[6:7], v[22:23], v[6:7]
	v_pk_mul_f32 v[22:23], v[86:87], v[0:1] op_sel_hi:[1,0]
	v_pk_mul_f32 v[12:13], v[20:21], v[12:13]
	v_pk_mul_f32 v[20:21], v[84:85], v[18:19] op_sel_hi:[1,0]
	v_pk_mul_f32 v[18:19], v[82:83], v[18:19] op_sel_hi:[1,0]
	v_pk_mul_f32 v[2:3], v[18:19], v[2:3]
	v_exp_f32_e64 v0, -v14
	v_exp_f32_e64 v18, -v15
	v_pk_mul_f32 v[10:11], v[22:23], v[10:11]
	v_pk_mul_f32 v[4:5], v[20:21], v[4:5]
	v_exp_f32_e64 v19, -v16
	v_exp_f32_e64 v20, -v17
	v_exp_f32_e64 v21, -v10
	v_add_f32_e32 v0, 1.0, v0
	v_exp_f32_e64 v22, -v11
	v_rcp_f32_e32 v0, v0
	v_add_f32_e32 v18, 1.0, v18
	v_exp_f32_e64 v23, -v12
	v_rcp_f32_e32 v18, v18
	v_add_f32_e32 v19, 1.0, v19
	v_exp_f32_e64 v24, -v13
	v_rcp_f32_e32 v19, v19
	v_add_f32_e32 v20, 1.0, v20
	v_rcp_f32_e32 v20, v20
	v_add_f32_e32 v21, 1.0, v21
	v_rcp_f32_e32 v21, v21
	v_add_f32_e32 v22, 1.0, v22
	v_mul_f32_e32 v0, v14, v0
	v_rcp_f32_e32 v22, v22
	v_add_f32_e32 v23, 1.0, v23
	v_mul_f32_e32 v0, v6, v0
	v_mul_f32_e32 v6, v15, v18
	v_rcp_f32_e32 v23, v23
	v_add_f32_e32 v24, 1.0, v24
	v_mul_f32_e32 v6, v7, v6
	v_mul_f32_e32 v7, v16, v19
	v_rcp_f32_e32 v24, v24
	v_mul_f32_e32 v7, v8, v7
	v_mul_f32_e32 v8, v17, v20
	v_mul_f32_e32 v8, v9, v8
	v_mul_f32_e32 v9, v10, v21
	v_mul_f32_e32 v9, v2, v9
	v_mul_f32_e32 v2, v11, v22
	v_mul_f32_e32 v3, v3, v2
	v_mul_f32_e32 v2, v12, v23
	v_mul_f32_e32 v4, v4, v2
	v_mul_f32_e32 v2, v13, v24
	v_mul_f32_e32 v5, v5, v2
	v_med3_f32 v0, v0, s23, v142
	v_med3_f32 v6, v6, s23, v142
	v_cvt_pk_fp8_f32 v2, v0, v6
	v_med3_f32 v0, v9, s23, v142
	v_med3_f32 v6, v3, s23, v142
	v_cvt_pk_fp8_f32 v3, v0, v6
	v_med3_f32 v7, v7, s23, v142
	v_med3_f32 v8, v8, s23, v142
	v_med3_f32 v4, v4, s23, v142
	v_med3_f32 v5, v5, s23, v142
	v_cvt_pk_fp8_f32 v2, v7, v8 op_sel:[0,0,1]
	v_cvt_pk_fp8_f32 v3, v4, v5 op_sel:[0,0,1]
	s_mov_b64 s[36:37], -1
	s_and_b64 vcc, exec, s[8:9]
	global_store_dwordx2 v[190:191], v[2:3], off
	s_cbranch_vccnz .LBB0_1491
	s_and_b64 vcc, exec, s[6:7]
	s_cbranch_vccnz .LBB0_1490
	s_barrier
	s_branch .LBB0_1490
